# c2pvq proj phase: preload all 32 weight fragments before barrier, counted vmcnt; linker-gap nop padding
# speedup vs baseline: 1.0182x; 1.0182x over previous
.LBB4_128:
	global_load_dwordx4 v[10:13], v[34:35], off offset:1120
	s_waitcnt vmcnt(0)
	v_pk_add_f32 v[8:9], v[8:9], v[10:11] neg_lo:[0,1] neg_hi:[0,1]
	v_pk_add_f32 v[2:3], v[2:3], v[12:13] neg_lo:[0,1] neg_hi:[0,1]
	s_or_b64 exec, exec, s[4:5]
	s_and_saveexec_b64 s[4:5], s[2:3]
	s_cbranch_execnz .LBB4_114
	s_branch .LBB4_115
	.p2align	8

.LBB5_63:
	s_load_dwordx8 s[40:47], s[0:1], 0x38
	s_load_dwordx2 s[8:9], s[0:1], 0x18
	s_load_dwordx2 s[6:7], s[0:1], 0x28
	s_bfe_u32 s10, s33, 0x20006
	s_waitcnt vmcnt(0)
	v_lshlrev_b64 v[34:35], 4, v[146:147]
	s_lshl_b32 s12, s10, 11
	s_waitcnt lgkmcnt(0)
	s_mov_b32 s13, 0
	v_add_u32_e32 v99, s12, v34
	s_mov_b32 s60, s8
	s_mov_b32 s61, s9
	global_load_dwordx4 v[100:103], v99, s[60:61] offset:16
	global_load_dwordx4 v[104:107], v99, s[60:61]
	s_add_u32 s60, s60, 0x2000
	s_addc_u32 s61, s61, 0
	global_load_dwordx4 v[108:111], v99, s[60:61] offset:16
	global_load_dwordx4 v[112:115], v99, s[60:61]
	s_add_u32 s60, s60, 0x2000
	s_addc_u32 s61, s61, 0
	global_load_dwordx4 v[116:119], v99, s[60:61] offset:16
	global_load_dwordx4 v[120:123], v99, s[60:61]
	s_add_u32 s60, s60, 0x2000
	s_addc_u32 s61, s61, 0
	global_load_dwordx4 v[124:127], v99, s[60:61] offset:16
	global_load_dwordx4 v[128:131], v99, s[60:61]
	s_add_u32 s60, s60, 0x2000
	s_addc_u32 s61, s61, 0
	global_load_dwordx4 v[136:139], v99, s[60:61] offset:16
	global_load_dwordx4 v[140:143], v99, s[60:61]
	s_add_u32 s60, s60, 0x2000
	s_addc_u32 s61, s61, 0
	global_load_dwordx4 v[156:159], v99, s[60:61] offset:16
	global_load_dwordx4 v[160:163], v99, s[60:61]
	s_add_u32 s60, s60, 0x2000
	s_addc_u32 s61, s61, 0
	global_load_dwordx4 v[164:167], v99, s[60:61] offset:16
	global_load_dwordx4 v[168:171], v99, s[60:61]
	s_add_u32 s60, s60, 0x2000
	s_addc_u32 s61, s61, 0
	global_load_dwordx4 v[172:175], v99, s[60:61] offset:16
	global_load_dwordx4 v[176:179], v99, s[60:61]
	s_add_u32 s60, s60, 0x2000
	s_addc_u32 s61, s61, 0
	global_load_dwordx4 v[180:183], v99, s[60:61] offset:16
	global_load_dwordx4 v[184:187], v99, s[60:61]
	s_add_u32 s60, s60, 0x2000
	s_addc_u32 s61, s61, 0
	global_load_dwordx4 v[188:191], v99, s[60:61] offset:16
	global_load_dwordx4 v[192:195], v99, s[60:61]
	s_add_u32 s60, s60, 0x2000
	s_addc_u32 s61, s61, 0
	global_load_dwordx4 v[196:199], v99, s[60:61] offset:16
	global_load_dwordx4 v[200:203], v99, s[60:61]
	s_add_u32 s60, s60, 0x2000
	s_addc_u32 s61, s61, 0
	global_load_dwordx4 v[204:207], v99, s[60:61] offset:16
	global_load_dwordx4 v[208:211], v99, s[60:61]
	s_add_u32 s60, s60, 0x2000
	s_addc_u32 s61, s61, 0
	global_load_dwordx4 v[212:215], v99, s[60:61] offset:16
	global_load_dwordx4 v[216:219], v99, s[60:61]
	s_add_u32 s60, s60, 0x2000
	s_addc_u32 s61, s61, 0
	global_load_dwordx4 v[220:223], v99, s[60:61] offset:16
	global_load_dwordx4 v[224:227], v99, s[60:61]
	s_add_u32 s60, s60, 0x2000
	s_addc_u32 s61, s61, 0
	global_load_dwordx4 v[228:231], v99, s[60:61] offset:16
	global_load_dwordx4 v[232:235], v99, s[60:61]
	s_add_u32 s60, s60, 0x2000
	s_addc_u32 s61, s61, 0
	global_load_dwordx4 v[236:239], v99, s[60:61] offset:16
	global_load_dwordx4 v[240:243], v99, s[60:61]
	s_barrier
	s_lshr_b32 s8, s33, 2
	s_and_b32 s8, s8, 0x3fffffc0
	s_movk_i32 s9, 0x110
	v_or_b32_e32 v38, s8, v150
	v_mul_lo_u32 v39, v38, s9
	v_add_u32_e32 v132, v152, v39
	v_add_u32_e32 v133, 0x2200, v132
	v_add_u32_e32 v144, 0x11000, v132
	v_add_u32_e32 v145, 0x11000, v133
	ds_read_b128 v[40:43], v132
	ds_read_b128 v[44:47], v132 offset:16
	ds_read_b128 v[48:51], v133
	ds_read_b128 v[52:55], v133 offset:16
	v_mov_b32_e32 v75, 0
	s_lshl_b32 s50, s5, 2
	s_mov_b32 s51, s13
	v_lshl_add_u64 v[76:77], s[6:7], 0, v[34:35]
	s_lshl_b64 s[6:7], s[50:51], 11
	v_mov_b32_e32 v82, 0xff7fc99e
	s_brev_b32 s14, 35
	v_mov_b32_e32 v84, 0xff7fc99e
	v_mov_b32_e32 v86, 0xff7fc99e
	v_mov_b32_e32 v87, 0xff7fc99e
	v_mov_b32_e32 v88, 0xff7fc99e
	v_mov_b32_e32 v90, 0xff7fc99e
	v_mov_b32_e32 v91, 0xff7fc99e
	v_mov_b32_e32 v92, 0xff7fc99e
	v_mov_b32_e32 v94, 0xff7fc99e
	v_mov_b32_e32 v95, 0xff7fc99e
	v_mov_b32_e32 v97, 0xff7fc99e
	v_mov_b32_e32 v80, v75
	v_mov_b32_e32 v81, v75
	v_mov_b32_e32 v83, 0xff7fc99e
	v_mov_b32_e32 v98, 0xff7fc99e
	v_mov_b32_e32 v93, 0xff7fc99e
	v_mov_b32_e32 v89, 0xff7fc99e
	v_mov_b32_e32 v85, 0xff7fc99e
	s_mov_b32 s15, 0
	ds_read_b128 v[56:59], v132 offset:64
	ds_read_b128 v[60:63], v132 offset:80
	ds_read_b128 v[64:67], v133 offset:64
	ds_read_b128 v[68:71], v133 offset:80
	s_waitcnt vmcnt(31) lgkmcnt(7)
	v_mfma_f32_32x32x16_f16 v[18:33], v[100:103], v[40:43], 0
	s_waitcnt lgkmcnt(5)
	v_mfma_f32_32x32x16_f16 v[2:17], v[100:103], v[48:51], 0
	s_waitcnt vmcnt(30) lgkmcnt(4)
	v_mfma_f32_32x32x16_f16 v[18:33], v[104:107], v[44:47], v[18:33]
	v_mfma_f32_32x32x16_f16 v[2:17], v[104:107], v[52:55], v[2:17]
	v_mfma_f32_32x32x16_f16 v[18:33], v[104:107], v[40:43], v[18:33]
	v_mfma_f32_32x32x16_f16 v[2:17], v[104:107], v[48:51], v[2:17]
	ds_read_b128 v[40:43], v132 offset:128
	ds_read_b128 v[44:47], v132 offset:144
	ds_read_b128 v[48:51], v133 offset:128
	ds_read_b128 v[52:55], v133 offset:144
	s_waitcnt vmcnt(29) lgkmcnt(7)
	v_mfma_f32_32x32x16_f16 v[18:33], v[108:111], v[56:59], v[18:33]
	s_waitcnt lgkmcnt(5)
	v_mfma_f32_32x32x16_f16 v[2:17], v[108:111], v[64:67], v[2:17]
	s_waitcnt vmcnt(28) lgkmcnt(4)
	v_mfma_f32_32x32x16_f16 v[18:33], v[112:115], v[60:63], v[18:33]
	v_mfma_f32_32x32x16_f16 v[2:17], v[112:115], v[68:71], v[2:17]
	v_mfma_f32_32x32x16_f16 v[18:33], v[112:115], v[56:59], v[18:33]
	v_mfma_f32_32x32x16_f16 v[2:17], v[112:115], v[64:67], v[2:17]
	ds_read_b128 v[56:59], v132 offset:192
	ds_read_b128 v[60:63], v132 offset:208
	ds_read_b128 v[64:67], v133 offset:192
	ds_read_b128 v[68:71], v133 offset:208
	s_waitcnt vmcnt(27) lgkmcnt(7)
	v_mfma_f32_32x32x16_f16 v[18:33], v[116:119], v[40:43], v[18:33]
	s_waitcnt lgkmcnt(5)
	v_mfma_f32_32x32x16_f16 v[2:17], v[116:119], v[48:51], v[2:17]
	s_waitcnt vmcnt(26) lgkmcnt(4)
	v_mfma_f32_32x32x16_f16 v[18:33], v[120:123], v[44:47], v[18:33]
	v_mfma_f32_32x32x16_f16 v[2:17], v[120:123], v[52:55], v[2:17]
	v_mfma_f32_32x32x16_f16 v[18:33], v[120:123], v[40:43], v[18:33]
	v_mfma_f32_32x32x16_f16 v[2:17], v[120:123], v[48:51], v[2:17]
	ds_read_b128 v[40:43], v132 offset:34816
	ds_read_b128 v[44:47], v132 offset:34832
	ds_read_b128 v[48:51], v133 offset:34816
	ds_read_b128 v[52:55], v133 offset:34832
	s_waitcnt vmcnt(25) lgkmcnt(7)
	v_mfma_f32_32x32x16_f16 v[18:33], v[124:127], v[56:59], v[18:33]
	s_waitcnt lgkmcnt(5)
	v_mfma_f32_32x32x16_f16 v[2:17], v[124:127], v[64:67], v[2:17]
	s_waitcnt vmcnt(24) lgkmcnt(4)
	v_mfma_f32_32x32x16_f16 v[18:33], v[128:131], v[60:63], v[18:33]
	v_mfma_f32_32x32x16_f16 v[2:17], v[128:131], v[68:71], v[2:17]
	v_mfma_f32_32x32x16_f16 v[18:33], v[128:131], v[56:59], v[18:33]
	v_mfma_f32_32x32x16_f16 v[2:17], v[128:131], v[64:67], v[2:17]
	ds_read_b128 v[56:59], v132 offset:34880
	ds_read_b128 v[60:63], v132 offset:34896
	ds_read_b128 v[64:67], v133 offset:34880
	ds_read_b128 v[68:71], v133 offset:34896
	s_waitcnt vmcnt(23) lgkmcnt(7)
	v_mfma_f32_32x32x16_f16 v[18:33], v[136:139], v[40:43], v[18:33]
	s_waitcnt lgkmcnt(5)
	v_mfma_f32_32x32x16_f16 v[2:17], v[136:139], v[48:51], v[2:17]
	s_waitcnt vmcnt(22) lgkmcnt(4)
	v_mfma_f32_32x32x16_f16 v[18:33], v[140:143], v[44:47], v[18:33]
	v_mfma_f32_32x32x16_f16 v[2:17], v[140:143], v[52:55], v[2:17]
	v_mfma_f32_32x32x16_f16 v[18:33], v[140:143], v[40:43], v[18:33]
	v_mfma_f32_32x32x16_f16 v[2:17], v[140:143], v[48:51], v[2:17]
	ds_read_b128 v[40:43], v132 offset:34944
	ds_read_b128 v[44:47], v132 offset:34960
	ds_read_b128 v[48:51], v133 offset:34944
	ds_read_b128 v[52:55], v133 offset:34960
	s_waitcnt vmcnt(21) lgkmcnt(7)
	v_mfma_f32_32x32x16_f16 v[18:33], v[156:159], v[56:59], v[18:33]
	s_waitcnt lgkmcnt(5)
	v_mfma_f32_32x32x16_f16 v[2:17], v[156:159], v[64:67], v[2:17]
	s_waitcnt vmcnt(20) lgkmcnt(4)
	v_mfma_f32_32x32x16_f16 v[18:33], v[160:163], v[60:63], v[18:33]
	v_mfma_f32_32x32x16_f16 v[2:17], v[160:163], v[68:71], v[2:17]
	v_mfma_f32_32x32x16_f16 v[18:33], v[160:163], v[56:59], v[18:33]
	v_mfma_f32_32x32x16_f16 v[2:17], v[160:163], v[64:67], v[2:17]
	ds_read_b128 v[56:59], v132 offset:35008
	ds_read_b128 v[60:63], v132 offset:35024
	ds_read_b128 v[64:67], v133 offset:35008
	ds_read_b128 v[68:71], v133 offset:35024
	s_waitcnt vmcnt(19) lgkmcnt(7)
	v_mfma_f32_32x32x16_f16 v[18:33], v[164:167], v[40:43], v[18:33]
	s_waitcnt lgkmcnt(5)
	v_mfma_f32_32x32x16_f16 v[2:17], v[164:167], v[48:51], v[2:17]
	s_waitcnt vmcnt(18) lgkmcnt(4)
	v_mfma_f32_32x32x16_f16 v[18:33], v[168:171], v[44:47], v[18:33]
	v_mfma_f32_32x32x16_f16 v[2:17], v[168:171], v[52:55], v[2:17]
	v_mfma_f32_32x32x16_f16 v[18:33], v[168:171], v[40:43], v[18:33]
	v_mfma_f32_32x32x16_f16 v[2:17], v[168:171], v[48:51], v[2:17]
	ds_read_b128 v[40:43], v144
	ds_read_b128 v[44:47], v144 offset:16
	ds_read_b128 v[48:51], v145
	ds_read_b128 v[52:55], v145 offset:16
	s_waitcnt vmcnt(17) lgkmcnt(7)
	v_mfma_f32_32x32x16_f16 v[18:33], v[172:175], v[56:59], v[18:33]
	s_waitcnt lgkmcnt(5)
	v_mfma_f32_32x32x16_f16 v[2:17], v[172:175], v[64:67], v[2:17]
	s_waitcnt vmcnt(16) lgkmcnt(4)
	v_mfma_f32_32x32x16_f16 v[18:33], v[176:179], v[60:63], v[18:33]
	v_mfma_f32_32x32x16_f16 v[2:17], v[176:179], v[68:71], v[2:17]
	v_mfma_f32_32x32x16_f16 v[18:33], v[176:179], v[56:59], v[18:33]
	v_mfma_f32_32x32x16_f16 v[2:17], v[176:179], v[64:67], v[2:17]
	ds_read_b128 v[56:59], v144 offset:64
	ds_read_b128 v[60:63], v144 offset:80
	ds_read_b128 v[64:67], v145 offset:64
	ds_read_b128 v[68:71], v145 offset:80
	s_waitcnt vmcnt(15) lgkmcnt(7)
	v_mfma_f32_32x32x16_f16 v[18:33], v[180:183], v[40:43], v[18:33]
	s_waitcnt lgkmcnt(5)
	v_mfma_f32_32x32x16_f16 v[2:17], v[180:183], v[48:51], v[2:17]
	s_waitcnt vmcnt(14) lgkmcnt(4)
	v_mfma_f32_32x32x16_f16 v[18:33], v[184:187], v[44:47], v[18:33]
	v_mfma_f32_32x32x16_f16 v[2:17], v[184:187], v[52:55], v[2:17]
	v_mfma_f32_32x32x16_f16 v[18:33], v[184:187], v[40:43], v[18:33]
	v_mfma_f32_32x32x16_f16 v[2:17], v[184:187], v[48:51], v[2:17]
	ds_read_b128 v[40:43], v144 offset:128
	ds_read_b128 v[44:47], v144 offset:144
	ds_read_b128 v[48:51], v145 offset:128
	ds_read_b128 v[52:55], v145 offset:144
	s_waitcnt vmcnt(13) lgkmcnt(7)
	v_mfma_f32_32x32x16_f16 v[18:33], v[188:191], v[56:59], v[18:33]
	s_waitcnt lgkmcnt(5)
	v_mfma_f32_32x32x16_f16 v[2:17], v[188:191], v[64:67], v[2:17]
	s_waitcnt vmcnt(12) lgkmcnt(4)
	v_mfma_f32_32x32x16_f16 v[18:33], v[192:195], v[60:63], v[18:33]
	v_mfma_f32_32x32x16_f16 v[2:17], v[192:195], v[68:71], v[2:17]
	v_mfma_f32_32x32x16_f16 v[18:33], v[192:195], v[56:59], v[18:33]
	v_mfma_f32_32x32x16_f16 v[2:17], v[192:195], v[64:67], v[2:17]
	ds_read_b128 v[56:59], v144 offset:192
	ds_read_b128 v[60:63], v144 offset:208
	ds_read_b128 v[64:67], v145 offset:192
	ds_read_b128 v[68:71], v145 offset:208
	s_waitcnt vmcnt(11) lgkmcnt(7)
	v_mfma_f32_32x32x16_f16 v[18:33], v[196:199], v[40:43], v[18:33]
	s_waitcnt lgkmcnt(5)
	v_mfma_f32_32x32x16_f16 v[2:17], v[196:199], v[48:51], v[2:17]
	s_waitcnt vmcnt(10) lgkmcnt(4)
	v_mfma_f32_32x32x16_f16 v[18:33], v[200:203], v[44:47], v[18:33]
	v_mfma_f32_32x32x16_f16 v[2:17], v[200:203], v[52:55], v[2:17]
	v_mfma_f32_32x32x16_f16 v[18:33], v[200:203], v[40:43], v[18:33]
	v_mfma_f32_32x32x16_f16 v[2:17], v[200:203], v[48:51], v[2:17]
	ds_read_b128 v[40:43], v144 offset:34816
	ds_read_b128 v[44:47], v144 offset:34832
	ds_read_b128 v[48:51], v145 offset:34816
	ds_read_b128 v[52:55], v145 offset:34832
	s_waitcnt vmcnt(9) lgkmcnt(7)
	v_mfma_f32_32x32x16_f16 v[18:33], v[204:207], v[56:59], v[18:33]
	s_waitcnt lgkmcnt(5)
	v_mfma_f32_32x32x16_f16 v[2:17], v[204:207], v[64:67], v[2:17]
	s_waitcnt vmcnt(8) lgkmcnt(4)
	v_mfma_f32_32x32x16_f16 v[18:33], v[208:211], v[60:63], v[18:33]
	v_mfma_f32_32x32x16_f16 v[2:17], v[208:211], v[68:71], v[2:17]
	v_mfma_f32_32x32x16_f16 v[18:33], v[208:211], v[56:59], v[18:33]
	v_mfma_f32_32x32x16_f16 v[2:17], v[208:211], v[64:67], v[2:17]
	ds_read_b128 v[56:59], v144 offset:34880
	ds_read_b128 v[60:63], v144 offset:34896
	ds_read_b128 v[64:67], v145 offset:34880
	ds_read_b128 v[68:71], v145 offset:34896
	s_waitcnt vmcnt(7) lgkmcnt(7)
	v_mfma_f32_32x32x16_f16 v[18:33], v[212:215], v[40:43], v[18:33]
	s_waitcnt lgkmcnt(5)
	v_mfma_f32_32x32x16_f16 v[2:17], v[212:215], v[48:51], v[2:17]
	s_waitcnt vmcnt(6) lgkmcnt(4)
	v_mfma_f32_32x32x16_f16 v[18:33], v[216:219], v[44:47], v[18:33]
	v_mfma_f32_32x32x16_f16 v[2:17], v[216:219], v[52:55], v[2:17]
	v_mfma_f32_32x32x16_f16 v[18:33], v[216:219], v[40:43], v[18:33]
	v_mfma_f32_32x32x16_f16 v[2:17], v[216:219], v[48:51], v[2:17]
	ds_read_b128 v[40:43], v144 offset:34944
	ds_read_b128 v[44:47], v144 offset:34960
	ds_read_b128 v[48:51], v145 offset:34944
	ds_read_b128 v[52:55], v145 offset:34960
	s_waitcnt vmcnt(5) lgkmcnt(7)
	v_mfma_f32_32x32x16_f16 v[18:33], v[220:223], v[56:59], v[18:33]
	s_waitcnt lgkmcnt(5)
	v_mfma_f32_32x32x16_f16 v[2:17], v[220:223], v[64:67], v[2:17]
	s_waitcnt vmcnt(4) lgkmcnt(4)
	v_mfma_f32_32x32x16_f16 v[18:33], v[224:227], v[60:63], v[18:33]
	v_mfma_f32_32x32x16_f16 v[2:17], v[224:227], v[68:71], v[2:17]
	v_mfma_f32_32x32x16_f16 v[18:33], v[224:227], v[56:59], v[18:33]
	v_mfma_f32_32x32x16_f16 v[2:17], v[224:227], v[64:67], v[2:17]
	ds_read_b128 v[56:59], v144 offset:35008
	ds_read_b128 v[60:63], v144 offset:35024
	ds_read_b128 v[64:67], v145 offset:35008
	ds_read_b128 v[68:71], v145 offset:35024
	s_waitcnt vmcnt(3) lgkmcnt(7)
	v_mfma_f32_32x32x16_f16 v[18:33], v[228:231], v[40:43], v[18:33]
	s_waitcnt lgkmcnt(5)
	v_mfma_f32_32x32x16_f16 v[2:17], v[228:231], v[48:51], v[2:17]
	s_waitcnt vmcnt(2) lgkmcnt(4)
	v_mfma_f32_32x32x16_f16 v[18:33], v[232:235], v[44:47], v[18:33]
	v_mfma_f32_32x32x16_f16 v[2:17], v[232:235], v[52:55], v[2:17]
	v_mfma_f32_32x32x16_f16 v[18:33], v[232:235], v[40:43], v[18:33]
	s_lshl_b32 s8, s10, 5
	v_or_b32_e32 v74, s8, v134
	s_waitcnt vmcnt(0)
	v_lshl_add_u64 v[36:37], v[74:75], 2, s[24:25]
	s_waitcnt lgkmcnt(0)
	s_barrier
	v_add_u32_e32 v74, s8, v134
	v_mfma_f32_32x32x16_f16 v[2:17], v[232:235], v[48:51], v[2:17]
	global_load_dwordx4 v[48:51], v[36:37], off
	v_lshl_add_u64 v[36:37], v[74:75], 2, s[24:25]
	global_load_dwordx4 v[52:55], v[36:37], off offset:32
	s_mov_b32 s8, 0x3a800000
	v_mov_b32_e32 v74, v75
	s_waitcnt vmcnt(3)
	v_mfma_f32_32x32x16_f16 v[18:33], v[236:239], v[56:59], v[18:33]
	s_waitcnt vmcnt(2)
	v_mfma_f32_32x32x16_f16 v[18:33], v[240:243], v[60:63], v[18:33]
	v_lshl_add_u32 v62, s10, 7, v135
	s_mov_b32 s10, 0x41800000
	v_mov_b32_e32 v135, v75
	v_lshl_add_u64 v[78:79], v[134:135], 2, s[22:23]
	v_mfma_f32_32x32x16_f16 v[2:17], v[236:239], v[64:67], v[2:17]
	v_mfma_f32_32x32x16_f16 v[18:33], v[240:243], v[56:59], v[18:33]
	global_load_dwordx4 v[56:59], v[36:37], off offset:64
	v_mfma_f32_32x32x16_f16 v[2:17], v[240:243], v[68:71], v[2:17]
	s_waitcnt vmcnt(2)
	s_nop 8
	v_fma_f32 v18, v18, s8, v48
	v_fma_f32 v19, v19, s8, v49
	v_fma_f32 v20, v20, s8, v50
	v_fma_f32 v21, v21, s8, v51
	v_pk_mul_f32 v[60:61], v[18:19], s[10:11] op_sel_hi:[1,0]
	v_pk_mul_f32 v[46:47], v[20:21], s[10:11] op_sel_hi:[1,0]
	v_cvt_pk_f16_f32 v60, v60, v61
	v_cvt_f32_f16_e32 v44, v60
	v_cvt_f32_f16_sdwa v45, v60 dst_sel:DWORD dst_unused:UNUSED_PAD src0_sel:WORD_1
	v_mfma_f32_32x32x16_f16 v[2:17], v[240:243], v[64:67], v[2:17]
	v_cvt_pk_f16_f32 v61, v46, v47
	v_cvt_f32_f16_e32 v46, v61
	v_cvt_f32_f16_sdwa v47, v61 dst_sel:DWORD dst_unused:UNUSED_PAD src0_sel:WORD_1
	v_fma_f32 v18, v18, s10, -v44
	v_fma_f32 v19, v19, s10, -v45
	s_movk_i32 s9, 0x210
	v_cvt_pk_f16_f32 v44, v18, v19
	v_pk_fma_f32 v[18:19], v[20:21], s[10:11], v[46:47] op_sel_hi:[1,0,1] neg_lo:[0,0,1] neg_hi:[0,0,1]
	s_nop 3
	v_pk_fma_f32 v[2:3], v[2:3], s[8:9], v[48:49] op_sel_hi:[1,0,1]
	v_cvt_pk_f16_f32 v45, v18, v19
	v_pk_mul_f32 v[18:19], v[2:3], s[10:11] op_sel_hi:[1,0]
	v_mul_lo_u32 v46, v38, s9
	v_cvt_pk_f16_f32 v38, v18, v19
	global_load_dwordx4 v[18:21], v[36:37], off offset:96
	v_pk_fma_f32 v[4:5], v[4:5], s[8:9], v[50:51] op_sel_hi:[1,0,1]
	v_cvt_f32_f16_e32 v40, v38
	v_pk_mul_f32 v[36:37], v[4:5], s[10:11] op_sel_hi:[1,0]
	v_cvt_f32_f16_sdwa v41, v38 dst_sel:DWORD dst_unused:UNUSED_PAD src0_sel:WORD_1
	v_cvt_pk_f16_f32 v39, v36, v37
	v_cvt_f32_f16_e32 v36, v39
	v_cvt_f32_f16_sdwa v37, v39 dst_sel:DWORD dst_unused:UNUSED_PAD src0_sel:WORD_1
	v_pk_fma_f32 v[2:3], v[2:3], s[10:11], v[40:41] op_sel_hi:[1,0,1] neg_lo:[0,0,1] neg_hi:[0,0,1]
	v_add_u32_e32 v40, 0x4200, v46
	v_cvt_pk_f16_f32 v2, v2, v3
	v_pk_fma_f32 v[4:5], v[4:5], s[10:11], v[36:37] op_sel_hi:[1,0,1] neg_lo:[0,0,1] neg_hi:[0,0,1]
	s_waitcnt vmcnt(2)
	v_pk_fma_f32 v[24:25], v[24:25], s[8:9], v[54:55] op_sel_hi:[1,0,1]
	v_cvt_pk_f16_f32 v3, v4, v5
	v_add_u32_e32 v4, v62, v40
	ds_write2_b64 v4, v[38:39], v[2:3] offset1:2
	v_pk_fma_f32 v[2:3], v[22:23], s[8:9], v[52:53] op_sel_hi:[1,0,1]
	v_pk_mul_f32 v[36:37], v[24:25], s[10:11] op_sel_hi:[1,0]
	v_pk_mul_f32 v[4:5], v[2:3], s[10:11] op_sel_hi:[1,0]
	v_pk_fma_f32 v[6:7], v[6:7], s[8:9], v[52:53] op_sel_hi:[1,0,1]
	v_cvt_pk_f16_f32 v4, v4, v5
	v_cvt_pk_f16_f32 v5, v36, v37
	v_cvt_f32_f16_e32 v22, v4
	v_cvt_f32_f16_sdwa v23, v4 dst_sel:DWORD dst_unused:UNUSED_PAD src0_sel:WORD_1
	v_cvt_f32_f16_e32 v36, v5
	v_cvt_f32_f16_sdwa v37, v5 dst_sel:DWORD dst_unused:UNUSED_PAD src0_sel:WORD_1
	v_pk_fma_f32 v[8:9], v[8:9], s[8:9], v[54:55] op_sel_hi:[1,0,1]
	v_pk_fma_f32 v[2:3], v[2:3], s[10:11], v[22:23] op_sel_hi:[1,0,1] neg_lo:[0,0,1] neg_hi:[0,0,1]
	v_add_u32_e32 v38, 32, v62
	v_pk_fma_f32 v[22:23], v[24:25], s[10:11], v[36:37] op_sel_hi:[1,0,1] neg_lo:[0,0,1] neg_hi:[0,0,1]
	v_cvt_pk_f16_f32 v2, v2, v3
	v_cvt_pk_f16_f32 v3, v22, v23
	v_pk_mul_f32 v[22:23], v[6:7], s[10:11] op_sel_hi:[1,0]
	v_pk_mul_f32 v[36:37], v[8:9], s[10:11] op_sel_hi:[1,0]
	v_cvt_pk_f16_f32 v22, v22, v23
	v_cvt_pk_f16_f32 v23, v36, v37
	v_cvt_f32_f16_e32 v24, v22
	v_cvt_f32_f16_sdwa v25, v22 dst_sel:DWORD dst_unused:UNUSED_PAD src0_sel:WORD_1
	v_cvt_f32_f16_e32 v36, v23
	v_cvt_f32_f16_sdwa v37, v23 dst_sel:DWORD dst_unused:UNUSED_PAD src0_sel:WORD_1
	v_add_u32_e32 v39, v38, v46
	ds_write2_b64 v39, v[4:5], v[2:3] offset1:2
	v_pk_fma_f32 v[2:3], v[6:7], s[10:11], v[24:25] op_sel_hi:[1,0,1] neg_lo:[0,0,1] neg_hi:[0,0,1]
	v_pk_fma_f32 v[4:5], v[8:9], s[10:11], v[36:37] op_sel_hi:[1,0,1] neg_lo:[0,0,1] neg_hi:[0,0,1]
	v_cvt_pk_f16_f32 v2, v2, v3
	v_cvt_pk_f16_f32 v3, v4, v5
	v_add_u32_e32 v4, v38, v40
	ds_write2_b64 v4, v[22:23], v[2:3] offset1:2
	v_add_u32_e32 v24, 64, v62
	v_add_u32_e32 v25, v24, v46
	v_add_u32_e32 v47, v62, v46
	ds_write2_b64 v47, v[60:61], v[44:45] offset1:2
	s_waitcnt vmcnt(1)
	v_pk_fma_f32 v[2:3], v[26:27], s[8:9], v[56:57] op_sel_hi:[1,0,1]
	v_pk_fma_f32 v[8:9], v[28:29], s[8:9], v[58:59] op_sel_hi:[1,0,1]
	v_pk_mul_f32 v[4:5], v[2:3], s[10:11] op_sel_hi:[1,0]
	v_pk_mul_f32 v[22:23], v[8:9], s[10:11] op_sel_hi:[1,0]
	v_cvt_pk_f16_f32 v4, v4, v5
	v_cvt_pk_f16_f32 v5, v22, v23
	v_cvt_f32_f16_e32 v6, v4
	v_cvt_f32_f16_sdwa v7, v4 dst_sel:DWORD dst_unused:UNUSED_PAD src0_sel:WORD_1
	v_cvt_f32_f16_e32 v22, v5
	v_cvt_f32_f16_sdwa v23, v5 dst_sel:DWORD dst_unused:UNUSED_PAD src0_sel:WORD_1
	v_pk_fma_f32 v[12:13], v[12:13], s[8:9], v[58:59] op_sel_hi:[1,0,1]
	v_pk_fma_f32 v[2:3], v[2:3], s[10:11], v[6:7] op_sel_hi:[1,0,1] neg_lo:[0,0,1] neg_hi:[0,0,1]
	v_mad_u32_u24 v96, v150, s9, v152
	v_pk_fma_f32 v[6:7], v[8:9], s[10:11], v[22:23] op_sel_hi:[1,0,1] neg_lo:[0,0,1] neg_hi:[0,0,1]
	v_cvt_pk_f16_f32 v2, v2, v3
	v_cvt_pk_f16_f32 v3, v6, v7
	v_pk_fma_f32 v[6:7], v[10:11], s[8:9], v[56:57] op_sel_hi:[1,0,1]
	v_pk_mul_f32 v[22:23], v[12:13], s[10:11] op_sel_hi:[1,0]
	v_pk_mul_f32 v[8:9], v[6:7], s[10:11] op_sel_hi:[1,0]
	ds_write2_b64 v25, v[4:5], v[2:3] offset1:2
	v_cvt_pk_f16_f32 v8, v8, v9
	v_cvt_pk_f16_f32 v9, v22, v23
	v_cvt_f32_f16_e32 v10, v8
	v_cvt_f32_f16_sdwa v11, v8 dst_sel:DWORD dst_unused:UNUSED_PAD src0_sel:WORD_1
	v_cvt_f32_f16_e32 v22, v9
	v_cvt_f32_f16_sdwa v23, v9 dst_sel:DWORD dst_unused:UNUSED_PAD src0_sel:WORD_1
	v_pk_fma_f32 v[2:3], v[6:7], s[10:11], v[10:11] op_sel_hi:[1,0,1] neg_lo:[0,0,1] neg_hi:[0,0,1]
	s_nop 0
	v_cvt_pk_f16_f32 v2, v2, v3
	v_pk_fma_f32 v[4:5], v[12:13], s[10:11], v[22:23] op_sel_hi:[1,0,1] neg_lo:[0,0,1] neg_hi:[0,0,1]
	s_waitcnt vmcnt(0)
	v_pk_fma_f32 v[12:13], v[16:17], s[8:9], v[20:21] op_sel_hi:[1,0,1]
	v_cvt_pk_f16_f32 v3, v4, v5
	v_add_u32_e32 v4, v24, v40
	ds_write2_b64 v4, v[8:9], v[2:3] offset1:2
	v_pk_fma_f32 v[2:3], v[30:31], s[8:9], v[18:19] op_sel_hi:[1,0,1]
	v_pk_fma_f32 v[8:9], v[32:33], s[8:9], v[20:21] op_sel_hi:[1,0,1]
	v_pk_mul_f32 v[4:5], v[2:3], s[10:11] op_sel_hi:[1,0]
	v_pk_mul_f32 v[10:11], v[8:9], s[10:11] op_sel_hi:[1,0]
	v_cvt_pk_f16_f32 v4, v4, v5
	v_cvt_pk_f16_f32 v5, v10, v11
	v_cvt_f32_f16_e32 v6, v4
	v_cvt_f32_f16_sdwa v7, v4 dst_sel:DWORD dst_unused:UNUSED_PAD src0_sel:WORD_1
	v_cvt_f32_f16_e32 v10, v5
	v_cvt_f32_f16_sdwa v11, v5 dst_sel:DWORD dst_unused:UNUSED_PAD src0_sel:WORD_1
	v_add_u32_e32 v22, 0x60, v62
	v_pk_fma_f32 v[2:3], v[2:3], s[10:11], v[6:7] op_sel_hi:[1,0,1] neg_lo:[0,0,1] neg_hi:[0,0,1]
	v_add_u32_e32 v23, v22, v46
	v_pk_fma_f32 v[6:7], v[8:9], s[10:11], v[10:11] op_sel_hi:[1,0,1] neg_lo:[0,0,1] neg_hi:[0,0,1]
	v_cvt_pk_f16_f32 v2, v2, v3
	v_cvt_pk_f16_f32 v3, v6, v7
	v_pk_fma_f32 v[6:7], v[14:15], s[8:9], v[18:19] op_sel_hi:[1,0,1]
	v_pk_mul_f32 v[14:15], v[12:13], s[10:11] op_sel_hi:[1,0]
	v_pk_mul_f32 v[8:9], v[6:7], s[10:11] op_sel_hi:[1,0]
	ds_write2_b64 v23, v[4:5], v[2:3] offset1:2
	v_cvt_pk_f16_f32 v8, v8, v9
	v_cvt_pk_f16_f32 v9, v14, v15
	v_cvt_f32_f16_e32 v10, v8
	v_cvt_f32_f16_sdwa v11, v8 dst_sel:DWORD dst_unused:UNUSED_PAD src0_sel:WORD_1
	v_cvt_f32_f16_e32 v14, v9
	v_cvt_f32_f16_sdwa v15, v9 dst_sel:DWORD dst_unused:UNUSED_PAD src0_sel:WORD_1
	v_pk_fma_f32 v[2:3], v[6:7], s[10:11], v[10:11] op_sel_hi:[1,0,1] neg_lo:[0,0,1] neg_hi:[0,0,1]
	s_nop 0
	v_cvt_pk_f16_f32 v2, v2, v3
	v_pk_fma_f32 v[4:5], v[12:13], s[10:11], v[14:15] op_sel_hi:[1,0,1] neg_lo:[0,0,1] neg_hi:[0,0,1]
	s_nop 0
	v_cvt_pk_f16_f32 v3, v4, v5
	v_add_u32_e32 v4, v22, v40
	ds_write2_b64 v4, v[8:9], v[2:3] offset1:2
	v_lshl_add_u64 v[2:3], v[76:77], 0, s[6:7]
	s_waitcnt lgkmcnt(0)
	s_barrier
	global_load_dwordx4 v[66:69], v[2:3], off
	global_load_dwordx4 v[70:73], v[2:3], off offset:16

.LBB5_141:
	v_mov_b32_e32 v2, v4
	s_waitcnt lgkmcnt(0)
	v_mov_b32_e32 v3, v5
	s_or_b64 exec, exec, s[6:7]
	s_and_saveexec_b64 s[6:7], s[8:9]
	s_cbranch_execnz .LBB5_98
	s_branch .LBB5_99
	.p2align	8

.LBB6_74:
	s_endpgm
	.p2align	8

	.text
	.p2alignl 6, 3212836864
	.fill 256, 4, 3212836864
	.p2alignl 8, 3212836864
